# E11 plus pipelined LDS transposition: each ds_write followed by its ds_read, stores issued as their vector lands
# speedup vs baseline: 1.0066x; 1.0013x over previous
.Lwarm_skip:
	s_or_b64 exec, exec, s[10:11]
	v_mad_u64_u32 v[2:3], s[6:7], v71, 12, s[6:7]
	v_lshlrev_b32_e32 v4, 2, v71
	v_mov_b32_e32 v5, v69
	s_movk_i32 s6, 0xfe00
	v_lshl_add_u64 v[4:5], s[8:9], 0, v[4:5]
	v_lshl_add_u64 v[8:9], v[2:3], 0, v[6:7]
	s_mov_b32 s7, -1
	v_lshl_add_u64 v[4:5], v[4:5], 0, v[6:7]
	v_lshl_add_u64 v[2:3], v[8:9], 0, s[6:7]
	v_cmp_gt_u32_e32 vcc, 32, v1
	v_lshlrev_b32_e32 v33, 12, v10
	v_add_u32_e32 v34, v33, v6
	v_cndmask_b32_e32 v3, v3, v5, vcc
	v_cndmask_b32_e32 v2, v2, v4, vcc
	global_load_dwordx4 v[2:5], v[2:3], off
	v_and_b32_e32 v72, 1, v0
	v_lshl_add_u32 v0, v32, 4, v33
	v_lshlrev_b32_e32 v73, 4, v32
	v_lshlrev_b32_e32 v74, 6, v72
	v_xor_b32_e32 v73, v73, v74
	v_lshl_add_u32 v73, v72, 11, v73
	v_lshl_add_u32 v73, v10, 12, v73
	v_and_b32_e32 v74, 31, v1
	v_lshrrev_b32_e32 v75, 5, v1
	v_lshl_or_b32 v76, v74, 2, v71
	v_lshlrev_b32_e32 v74, 4, v74
	v_lshlrev_b32_e32 v77, 6, v75
	v_xor_b32_e32 v74, v74, v77
	v_lshl_add_u32 v74, v75, 11, v74
	v_lshl_add_u32 v74, v10, 12, v74
	v_lshlrev_b32_e32 v77, 7, v71
	v_and_b32_e32 v77, 0xe000000, v77
	v_and_b32_e32 v76, 0x3fffc, v76
	v_lshlrev_b32_e32 v75, 21, v75
	v_or3_b32 v75, v77, v75, v76
	v_lshlrev_b32_e32 v75, 2, v75
	s_mul_i32 s6, s4, 0x138800
	s_mul_hi_i32 s5, s4, 0x138800
	s_add_u32 s2, s2, s6
	s_addc_u32 s3, s3, s5
	global_load_dwordx4 v[28:31], v[8:9], off offset:512
	s_waitcnt vmcnt(1)
	ds_write_b128 v34, v[2:5]
	ds_read_b128 v[4:7], v0
	v_lshlrev_b32_e32 v0, 4, v72
	s_waitcnt lgkmcnt(0)
	v_max_i32_e32 v1, 0, v4
	v_max_i32_e32 v2, 0, v5
	v_max_i32_e32 v3, 0, v6
	v_max_i32_e32 v8, 0, v7
	v_lshl_or_b32 v35, v1, 7, v0
	v_lshl_or_b32 v36, v2, 7, v0
	v_lshl_or_b32 v37, v3, 7, v0
	v_lshl_or_b32 v38, v8, 7, v0
	global_load_dwordx4 v[20:23], v35, s[2:3]
	global_load_dwordx4 v[16:19], v35, s[2:3] offset:32
	global_load_dwordx4 v[8:11], v35, s[2:3] offset:64
	global_load_dwordx4 v[64:67], v36, s[2:3]
	global_load_dwordx4 v[60:63], v36, s[2:3] offset:32
	global_load_dwordx4 v[56:59], v36, s[2:3] offset:64
	global_load_dwordx4 v[52:55], v37, s[2:3]
	global_load_dwordx4 v[48:51], v37, s[2:3] offset:32
	global_load_dwordx4 v[44:47], v37, s[2:3] offset:64
	global_load_dwordx4 v[24:27], v38, s[2:3]
	global_load_dwordx4 v[12:15], v38, s[2:3] offset:32
	global_load_dwordx4 v[0:3], v38, s[2:3] offset:64
	s_waitcnt vmcnt(12)
	ds_write_b128 v34, v[28:31] offset:1024
	v_mul_u32_u24_e32 v28, 48, v32
	v_cmp_lt_i32_e32 vcc, -1, v4
	v_add_u32_e32 v31, v33, v28
	v_mov_b32_e32 v28, 0
	s_and_saveexec_b64 s[2:3], vcc
	ds_read_b32 v28, v31 offset:512
	s_or_b64 exec, exec, s[2:3]
	s_and_saveexec_b64 s[2:3], vcc
	ds_read_b32 v69, v31 offset:516
	s_or_b64 exec, exec, s[2:3]
	v_mov_b32_e32 v29, 0
	v_mov_b32_e32 v4, 0
	s_and_saveexec_b64 s[2:3], vcc
	ds_read_b32 v4, v31 offset:520
	s_or_b64 exec, exec, s[2:3]
	s_waitcnt vmcnt(11) lgkmcnt(0)
	v_fma_mix_f32 v30, v28, v20, v29 op_sel_hi:[0,1,0]
	v_fma_mix_f32 v20, v28, v20, v29 op_sel:[0,1,0] op_sel_hi:[0,1,0]
	v_fma_mix_f32 v32, v28, v21, v29 op_sel_hi:[0,1,0]
	v_fma_mix_f32 v21, v28, v21, v29 op_sel:[0,1,0] op_sel_hi:[0,1,0]
	v_fma_mix_f32 v33, v28, v22, v29 op_sel_hi:[0,1,0]
	v_fma_mix_f32 v22, v28, v22, v29 op_sel:[0,1,0] op_sel_hi:[0,1,0]
	v_fma_mix_f32 v34, v28, v23, v29 op_sel_hi:[0,1,0]
	v_fma_mix_f32 v23, v28, v23, v29 op_sel:[0,1,0] op_sel_hi:[0,1,0]
	s_waitcnt vmcnt(10)
	v_fma_mix_f32 v28, v69, v16, v30 op_sel_hi:[0,1,0]
	v_fma_mix_f32 v16, v69, v16, v20 op_sel:[0,1,0] op_sel_hi:[0,1,0]
	v_fma_mix_f32 v20, v69, v17, v32 op_sel_hi:[0,1,0]
	v_cmp_lt_i32_e32 vcc, -1, v5
	v_fma_mix_f32 v17, v69, v17, v21 op_sel:[0,1,0] op_sel_hi:[0,1,0]
	v_fma_mix_f32 v21, v69, v18, v33 op_sel_hi:[0,1,0]
	v_fma_mix_f32 v18, v69, v18, v22 op_sel:[0,1,0] op_sel_hi:[0,1,0]
	v_fma_mix_f32 v22, v69, v19, v34 op_sel_hi:[0,1,0]
	v_fma_mix_f32 v19, v69, v19, v23 op_sel:[0,1,0] op_sel_hi:[0,1,0]
	s_waitcnt vmcnt(9)
	s_and_saveexec_b64 s[2:3], vcc
	ds_read_b32 v29, v31 offset:524
	s_or_b64 exec, exec, s[2:3]
	v_mov_b32_e32 v5, 0
	s_and_saveexec_b64 s[2:3], vcc
	ds_read_b32 v5, v31 offset:532
	s_or_b64 exec, exec, s[2:3]
	v_fma_mix_f32 v40, v4, v8, v28 op_sel_hi:[0,1,0]
	v_fma_mix_f32 v36, v4, v8, v16 op_sel:[0,1,0] op_sel_hi:[0,1,0]
	v_fma_mix_f32 v32, v4, v9, v20 op_sel_hi:[0,1,0]
	v_fma_mix_f32 v28, v4, v9, v17 op_sel:[0,1,0] op_sel_hi:[0,1,0]
	v_mov_b32_e32 v9, 0
	s_and_saveexec_b64 s[2:3], vcc
	ds_read_b32 v9, v31 offset:528
	s_or_b64 exec, exec, s[2:3]
	v_fma_mix_f32 v20, v4, v10, v21 op_sel_hi:[0,1,0]
	v_fma_mix_f32 v16, v4, v10, v18 op_sel:[0,1,0] op_sel_hi:[0,1,0]
	v_fma_mix_f32 v8, v4, v11, v22 op_sel_hi:[0,1,0]
	v_fma_mix_f32 v4, v4, v11, v19 op_sel:[0,1,0] op_sel_hi:[0,1,0]
	v_mov_b32_e32 v10, 0
	s_waitcnt vmcnt(8) lgkmcnt(0)
	v_fma_mix_f32 v18, v29, v65, v10 op_sel_hi:[0,1,0]
	v_fma_mix_f32 v17, v29, v64, v10 op_sel:[0,1,0] op_sel_hi:[0,1,0]
	v_fma_mix_f32 v21, v29, v66, v10 op_sel_hi:[0,1,0]
	v_fma_mix_f32 v11, v29, v64, v10 op_sel_hi:[0,1,0]
	v_fma_mix_f32 v19, v29, v65, v10 op_sel:[0,1,0] op_sel_hi:[0,1,0]
	s_waitcnt vmcnt(7)
	v_fma_mix_f32 v18, v9, v61, v18 op_sel_hi:[0,1,0]
	v_fma_mix_f32 v22, v29, v66, v10 op_sel:[0,1,0] op_sel_hi:[0,1,0]
	v_fma_mix_f32 v23, v29, v67, v10 op_sel_hi:[0,1,0]
	v_fma_mix_f32 v29, v29, v67, v10 op_sel:[0,1,0] op_sel_hi:[0,1,0]
	v_fma_mix_f32 v17, v9, v60, v17 op_sel:[0,1,0] op_sel_hi:[0,1,0]
	v_fma_mix_f32 v21, v9, v62, v21 op_sel_hi:[0,1,0]
	s_waitcnt vmcnt(6)
	v_fma_mix_f32 v33, v5, v57, v18 op_sel_hi:[0,1,0]
	v_cmp_lt_i32_e32 vcc, -1, v6
	v_mov_b32_e32 v18, 0
	s_and_saveexec_b64 s[2:3], vcc
	ds_read_b32 v18, v31 offset:536
	s_or_b64 exec, exec, s[2:3]
	s_and_saveexec_b64 s[2:3], vcc
	ds_read_b32 v10, v31 offset:540
	s_or_b64 exec, exec, s[2:3]
	v_mov_b32_e32 v6, 0
	s_and_saveexec_b64 s[2:3], vcc
	ds_read_b32 v6, v31 offset:544
	s_or_b64 exec, exec, s[2:3]
	v_fma_mix_f32 v11, v9, v60, v11 op_sel_hi:[0,1,0]
	v_fma_mix_f32 v19, v9, v61, v19 op_sel:[0,1,0] op_sel_hi:[0,1,0]
	v_fma_mix_f32 v22, v9, v62, v22 op_sel:[0,1,0] op_sel_hi:[0,1,0]
	v_fma_mix_f32 v23, v9, v63, v23 op_sel_hi:[0,1,0]
	v_fma_mix_f32 v30, v9, v63, v29 op_sel:[0,1,0] op_sel_hi:[0,1,0]
	v_fma_mix_f32 v37, v5, v56, v17 op_sel:[0,1,0] op_sel_hi:[0,1,0]
	s_nop 0
	v_fma_mix_f32 v41, v5, v56, v11 op_sel_hi:[0,1,0]
	v_fma_mix_f32 v29, v5, v57, v19 op_sel:[0,1,0] op_sel_hi:[0,1,0]
	v_fma_mix_f32 v21, v5, v58, v21 op_sel_hi:[0,1,0]
	v_fma_mix_f32 v17, v5, v58, v22 op_sel:[0,1,0] op_sel_hi:[0,1,0]
	v_fma_mix_f32 v9, v5, v59, v23 op_sel_hi:[0,1,0]
	v_fma_mix_f32 v5, v5, v59, v30 op_sel:[0,1,0] op_sel_hi:[0,1,0]
	v_mov_b32_e32 v11, 0
	s_waitcnt vmcnt(5) lgkmcnt(0)
	v_fma_mix_f32 v22, v18, v52, v11 op_sel:[0,1,0] op_sel_hi:[0,1,0]
	v_fma_mix_f32 v30, v18, v53, v11 op_sel:[0,1,0] op_sel_hi:[0,1,0]
	v_fma_mix_f32 v19, v18, v52, v11 op_sel_hi:[0,1,0]
	v_fma_mix_f32 v23, v18, v53, v11 op_sel_hi:[0,1,0]
	v_fma_mix_f32 v34, v18, v54, v11 op_sel_hi:[0,1,0]
	v_fma_mix_f32 v35, v18, v54, v11 op_sel:[0,1,0] op_sel_hi:[0,1,0]
	v_fma_mix_f32 v38, v18, v55, v11 op_sel_hi:[0,1,0]
	v_fma_mix_f32 v18, v18, v55, v11 op_sel:[0,1,0] op_sel_hi:[0,1,0]
	s_waitcnt vmcnt(4)
	v_fma_mix_f32 v22, v10, v48, v22 op_sel:[0,1,0] op_sel_hi:[0,1,0]
	v_fma_mix_f32 v30, v10, v49, v30 op_sel:[0,1,0] op_sel_hi:[0,1,0]
	v_cmp_lt_i32_e32 vcc, -1, v7
	s_and_saveexec_b64 s[2:3], vcc
	ds_read_b32 v11, v31 offset:548
	s_or_b64 exec, exec, s[2:3]
	v_mov_b32_e32 v7, 0
	s_and_saveexec_b64 s[2:3], vcc
	ds_read_b32 v7, v31 offset:556
	s_or_b64 exec, exec, s[2:3]
	v_fma_mix_f32 v19, v10, v48, v19 op_sel_hi:[0,1,0]
	v_fma_mix_f32 v23, v10, v49, v23 op_sel_hi:[0,1,0]
	v_fma_mix_f32 v39, v10, v50, v34 op_sel_hi:[0,1,0]
	v_fma_mix_f32 v35, v10, v50, v35 op_sel:[0,1,0] op_sel_hi:[0,1,0]
	v_fma_mix_f32 v43, v10, v51, v38 op_sel_hi:[0,1,0]
	v_fma_mix_f32 v48, v10, v51, v18 op_sel:[0,1,0] op_sel_hi:[0,1,0]
	s_waitcnt vmcnt(3)
	v_fma_mix_f32 v42, v6, v44, v19 op_sel_hi:[0,1,0]
	v_mov_b32_e32 v19, 0
	s_and_saveexec_b64 s[2:3], vcc
	ds_read_b32 v19, v31 offset:552
	s_or_b64 exec, exec, s[2:3]
	v_fma_mix_f32 v38, v6, v44, v22 op_sel:[0,1,0] op_sel_hi:[0,1,0]
	v_fma_mix_f32 v34, v6, v45, v23 op_sel_hi:[0,1,0]
	v_fma_mix_f32 v30, v6, v45, v30 op_sel:[0,1,0] op_sel_hi:[0,1,0]
	v_fma_mix_f32 v22, v6, v46, v39 op_sel_hi:[0,1,0]
	v_fma_mix_f32 v18, v6, v46, v35 op_sel:[0,1,0] op_sel_hi:[0,1,0]
	v_fma_mix_f32 v10, v6, v47, v43 op_sel_hi:[0,1,0]
	v_fma_mix_f32 v6, v6, v47, v48 op_sel:[0,1,0] op_sel_hi:[0,1,0]
	s_load_dwordx2 s[0:1], s[0:1], 0x18
	s_ashr_i32 s5, s4, 31
	v_mov_b32_e32 v23, 0
	s_waitcnt vmcnt(2) lgkmcnt(0)
	v_fma_mix_f32 v31, v11, v24, v23 op_sel_hi:[0,1,0]
	v_fma_mix_f32 v24, v11, v24, v23 op_sel:[0,1,0] op_sel_hi:[0,1,0]
	v_fma_mix_f32 v35, v11, v25, v23 op_sel_hi:[0,1,0]
	v_fma_mix_f32 v25, v11, v25, v23 op_sel:[0,1,0] op_sel_hi:[0,1,0]
	v_fma_mix_f32 v39, v11, v26, v23 op_sel_hi:[0,1,0]
	v_fma_mix_f32 v26, v11, v26, v23 op_sel:[0,1,0] op_sel_hi:[0,1,0]
	v_fma_mix_f32 v43, v11, v27, v23 op_sel_hi:[0,1,0]
	v_fma_mix_f32 v11, v11, v27, v23 op_sel:[0,1,0] op_sel_hi:[0,1,0]
	s_waitcnt vmcnt(1)
	v_fma_mix_f32 v23, v19, v12, v31 op_sel_hi:[0,1,0]
	s_lshl_b64 s[2:3], s[4:5], 24
	v_fma_mix_f32 v12, v19, v12, v24 op_sel:[0,1,0] op_sel_hi:[0,1,0]
	v_fma_mix_f32 v24, v19, v13, v35 op_sel_hi:[0,1,0]
	v_fma_mix_f32 v13, v19, v13, v25 op_sel:[0,1,0] op_sel_hi:[0,1,0]
	v_fma_mix_f32 v25, v19, v14, v39 op_sel_hi:[0,1,0]
	v_fma_mix_f32 v14, v19, v14, v26 op_sel:[0,1,0] op_sel_hi:[0,1,0]
	v_fma_mix_f32 v26, v19, v15, v43 op_sel_hi:[0,1,0]
	v_fma_mix_f32 v15, v19, v15, v11 op_sel:[0,1,0] op_sel_hi:[0,1,0]
	s_add_u32 s0, s0, s2
	s_addc_u32 s1, s1, s3
	s_add_u32 s2, s0, 0x100000
	s_addc_u32 s3, s1, 0
	s_add_u32 s4, s0, 0x200000
	s_addc_u32 s5, s1, 0
	s_add_u32 s6, s0, 0x300000
	s_addc_u32 s7, s1, 0
	s_add_u32 s8, s0, 0x400000
	s_addc_u32 s9, s1, 0
	s_add_u32 s10, s0, 0x500000
	s_addc_u32 s11, s1, 0
	s_add_u32 s12, s0, 0x600000
	s_addc_u32 s13, s1, 0
	s_add_u32 s14, s0, 0x700000
	s_addc_u32 s15, s1, 0
	s_waitcnt vmcnt(0)
	v_fma_mix_f32 v43, v7, v0, v23 op_sel_hi:[0,1,0]
	v_fma_mix_f32 v23, v7, v2, v25 op_sel_hi:[0,1,0]
	v_fma_mix_f32 v19, v7, v2, v14 op_sel:[0,1,0] op_sel_hi:[0,1,0]
	v_fma_mix_f32 v39, v7, v0, v12 op_sel:[0,1,0] op_sel_hi:[0,1,0]
	v_fma_mix_f32 v35, v7, v1, v24 op_sel_hi:[0,1,0]
	v_fma_mix_f32 v31, v7, v1, v13 op_sel:[0,1,0] op_sel_hi:[0,1,0]
	v_fma_mix_f32 v11, v7, v3, v26 op_sel_hi:[0,1,0]
	v_fma_mix_f32 v7, v7, v3, v15 op_sel:[0,1,0] op_sel_hi:[0,1,0]
	ds_write_b128 v73, v[40:43]
	ds_read_b128 v[44:47], v74
	ds_write_b128 v73, v[36:39] offset:512
	ds_read_b128 v[48:51], v74 offset:512
	ds_write_b128 v73, v[32:35] offset:1024
	ds_read_b128 v[52:55], v74 offset:1024
	ds_write_b128 v73, v[28:31] offset:1536
	ds_read_b128 v[56:59], v74 offset:1536
	s_waitcnt lgkmcnt(6)
	global_store_dwordx4 v75, v[44:47], s[0:1] nt
	ds_write_b128 v73, v[20:23]
	ds_read_b128 v[60:63], v74
	s_waitcnt lgkmcnt(6)
	global_store_dwordx4 v75, v[48:51], s[2:3] nt
	ds_write_b128 v73, v[16:19] offset:512
	ds_read_b128 v[64:67], v74 offset:512
	s_waitcnt lgkmcnt(6)
	global_store_dwordx4 v75, v[52:55], s[4:5] nt
	ds_write_b128 v73, v[8:11] offset:1024
	ds_read_b128 v[0:3], v74 offset:1024
	s_waitcnt lgkmcnt(6)
	global_store_dwordx4 v75, v[56:59], s[6:7] nt
	ds_write_b128 v73, v[4:7] offset:1536
	ds_read_b128 v[12:15], v74 offset:1536
	s_waitcnt lgkmcnt(6)
	global_store_dwordx4 v75, v[60:63], s[8:9] nt
	s_waitcnt lgkmcnt(4)
	global_store_dwordx4 v75, v[64:67], s[10:11] nt
	s_waitcnt lgkmcnt(2)
	global_store_dwordx4 v75, v[0:3], s[12:13] nt
	s_waitcnt lgkmcnt(0)
	global_store_dwordx4 v75, v[12:15], s[14:15] nt
	s_endpgm
